# Wo GEMM epilogue de-serialised: 16 residual-tile loads requested up front into separate registers, counted vmcnt(15) per block (was load + vmcnt(0) + store, 16 times in series); on top of the MoBA pro
# speedup vs baseline: 1.0227x; 1.0054x over previous
.LBB0_962:
	v_mov_b32_e32 v2, v0
	v_mov_b32_e32 v6, v0
	v_add_u32_e32 v2, s55, v2
	ds_read_b128 v[2:5], v2
	v_mov_b32_e32 v10, v0
	v_add_u32_e32 v6, s55, v6
	ds_read_b128 v[6:9], v6 offset:1024
	v_mov_b32_e32 v14, v0
	v_add_u32_e32 v10, s55, v10
	ds_read_b128 v[10:13], v10 offset:2048
	s_add_u32 s36, s34, 0x100
	v_add_u32_e32 v14, s55, v14
	s_addc_u32 s37, s35, 0
	ds_read_b128 v[14:17], v14 offset:3072
	s_cmp_eq_u32 s70, 4
	s_cselect_b32 s46, s66, s36
	s_cselect_b32 s47, s17, s37
	s_cselect_b32 s42, s67, s68
	s_cselect_b32 s43, s15, s69
	s_add_u32 s44, s46, 0x80
	s_addc_u32 s45, s47, 0
	v_mov_b32_e32 v148, v0
	v_mov_b32_e32 v152, v0
	v_add_u32_e32 v148, s56, v148
	ds_read_b128 v[148:151], v148
	v_mov_b32_e32 v156, v0
	v_add_u32_e32 v152, s56, v152
	ds_read_b128 v[152:155], v152 offset:1024
	v_mov_b32_e32 v160, v0
	v_add_u32_e32 v156, s56, v156
	ds_read_b128 v[156:159], v156 offset:2048
	v_mov_b32_e32 v164, v0
	v_add_u32_e32 v160, s56, v160
	ds_read_b128 v[160:163], v160 offset:3072
	v_mov_b32_e32 v168, v0
	v_add_u32_e32 v164, s56, v164
	ds_read_b128 v[164:167], v164 offset:4096
	v_mov_b32_e32 v172, v0
	v_add_u32_e32 v168, s56, v168
	ds_read_b128 v[168:171], v168 offset:5120
	v_mov_b32_e32 v176, v0
	v_add_u32_e32 v172, s56, v172
	s_add_u32 s34, s34, 0x20080
	ds_read_b128 v[172:175], v172 offset:6144
	s_addc_u32 s35, s35, 0
	v_add_u32_e32 v176, s56, v176
	s_mov_b64 s[76:77], s[34:35]
	v_mov_b32_e32 v180, v146
	s_add_i32 m0, s29, 0xc000
	ds_read_b128 v[176:179], v176 offset:7168
	s_add_u32 s34, s34, 0x10000
	global_load_lds_dwordx4 v180, s[76:77]
	s_addc_u32 s35, s35, 0
	v_mov_b32_e32 v180, v146
	s_add_i32 m0, s29, 0xe000
	s_nop 0
	global_load_lds_dwordx4 v180, s[34:35]
	s_waitcnt lgkmcnt(8)
	s_barrier
	s_waitcnt lgkmcnt(0)
	s_setprio 1
	s_waitcnt lgkmcnt(0)
	v_mfma_scale_f32_16x16x128_f8f6f4 v[142:145], v[2:9], v[148:155], v[142:145], v222, v222 op_sel:[0,1,0] op_sel_hi:[0,0,0]
	v_mfma_scale_f32_16x16x128_f8f6f4 v[138:141], v[10:17], v[148:155], v[138:141], v222, v222 op_sel:[0,1,0] op_sel_hi:[0,0,0]
	v_mfma_scale_f32_16x16x128_f8f6f4 v[126:129], v[2:9], v[156:163], v[126:129], v222, v222 op_sel:[0,1,0] op_sel_hi:[0,0,0]
	v_mfma_scale_f32_16x16x128_f8f6f4 v[122:125], v[10:17], v[156:163], v[122:125], v222, v222 op_sel:[0,1,0] op_sel_hi:[0,0,0]
	v_mfma_scale_f32_16x16x128_f8f6f4 v[110:113], v[2:9], v[164:171], v[110:113], v222, v222 op_sel:[0,1,0] op_sel_hi:[0,0,0]
	v_mfma_scale_f32_16x16x128_f8f6f4 v[106:109], v[10:17], v[164:171], v[106:109], v222, v222 op_sel:[0,1,0] op_sel_hi:[0,0,0]
	v_mfma_scale_f32_16x16x128_f8f6f4 v[94:97], v[2:9], v[172:179], v[94:97], v222, v222 op_sel:[0,1,0] op_sel_hi:[0,0,0]
	v_mfma_scale_f32_16x16x128_f8f6f4 v[90:93], v[10:17], v[172:179], v[90:93], v222, v222 op_sel:[0,1,0] op_sel_hi:[0,0,0]
	s_setprio 0
	s_barrier
	v_mov_b32_e32 v180, v0
	v_mov_b32_e32 v184, v0
	v_add_u32_e32 v180, s58, v180
	ds_read_b128 v[180:183], v180
	v_mov_b32_e32 v188, v0
	v_add_u32_e32 v184, s58, v184
	ds_read_b128 v[184:187], v184 offset:1024
	v_mov_b32_e32 v192, v0
	v_add_u32_e32 v188, s58, v188
	ds_read_b128 v[188:191], v188 offset:2048
	s_mov_b64 s[34:35], s[42:43]
	v_add_u32_e32 v192, s58, v192
	s_mov_b32 m0, s33
	ds_read_b128 v[192:195], v192 offset:3072
	v_mov_b32_e32 v196, v147
	s_nop 0
	global_load_lds_dwordx4 v196, s[34:35]
	s_add_u32 s34, s42, 0x10000
	s_addc_u32 s35, s43, 0
	v_mov_b32_e32 v196, v147
	s_mov_b32 m0, s38
	s_nop 0
	global_load_lds_dwordx4 v196, s[34:35]
	s_barrier
	s_waitcnt lgkmcnt(0)
	s_setprio 1
	s_waitcnt lgkmcnt(0)
	v_mfma_scale_f32_16x16x128_f8f6f4 v[134:137], v[180:187], v[148:155], v[134:137], v222, v222 op_sel:[0,1,0] op_sel_hi:[0,0,0]
	v_mfma_scale_f32_16x16x128_f8f6f4 v[130:133], v[188:195], v[148:155], v[130:133], v222, v222 op_sel:[0,1,0] op_sel_hi:[0,0,0]
	v_mfma_scale_f32_16x16x128_f8f6f4 v[118:121], v[180:187], v[156:163], v[118:121], v222, v222 op_sel:[0,1,0] op_sel_hi:[0,0,0]
	v_mfma_scale_f32_16x16x128_f8f6f4 v[114:117], v[188:195], v[156:163], v[114:117], v222, v222 op_sel:[0,1,0] op_sel_hi:[0,0,0]
	v_mfma_scale_f32_16x16x128_f8f6f4 v[102:105], v[180:187], v[164:171], v[102:105], v222, v222 op_sel:[0,1,0] op_sel_hi:[0,0,0]
	v_mfma_scale_f32_16x16x128_f8f6f4 v[98:101], v[188:195], v[164:171], v[98:101], v222, v222 op_sel:[0,1,0] op_sel_hi:[0,0,0]
	v_mfma_scale_f32_16x16x128_f8f6f4 v[86:89], v[180:187], v[172:179], v[86:89], v222, v222 op_sel:[0,1,0] op_sel_hi:[0,0,0]
	v_mfma_scale_f32_16x16x128_f8f6f4 v[82:85], v[188:195], v[172:179], v[82:85], v222, v222 op_sel:[0,1,0] op_sel_hi:[0,0,0]
	s_setprio 0
	v_mov_b32_e32 v148, v0
	s_barrier
	v_mov_b32_e32 v152, v0
	v_add_u32_e32 v148, s56, v148
	ds_read_b128 v[148:151], v148 offset:16384
	v_mov_b32_e32 v156, v0
	v_add_u32_e32 v152, s56, v152
	ds_read_b128 v[152:155], v152 offset:17408
	v_mov_b32_e32 v160, v0
	v_add_u32_e32 v156, s56, v156
	ds_read_b128 v[156:159], v156 offset:18432
	v_mov_b32_e32 v164, v0
	v_add_u32_e32 v160, s56, v160
	ds_read_b128 v[160:163], v160 offset:19456
	v_mov_b32_e32 v168, v0
	v_add_u32_e32 v164, s56, v164
	ds_read_b128 v[164:167], v164 offset:20480
	v_mov_b32_e32 v172, v0
	v_add_u32_e32 v168, s56, v168
	ds_read_b128 v[168:171], v168 offset:21504
	v_mov_b32_e32 v176, v0
	v_add_u32_e32 v172, s56, v172
	ds_read_b128 v[172:175], v172 offset:22528
	s_mov_b64 s[34:35], s[46:47]
	v_add_u32_e32 v176, s56, v176
	s_mov_b32 m0, s29
	ds_read_b128 v[176:179], v176 offset:23552
	v_mov_b32_e32 v196, v146
	s_nop 0
	global_load_lds_dwordx4 v196, s[34:35]
	s_add_u32 s34, s46, 0x10000
	s_addc_u32 s35, s47, 0
	v_mov_b32_e32 v196, v146
	s_mov_b32 m0, s39
	s_nop 0
	global_load_lds_dwordx4 v196, s[34:35]
	s_barrier
	s_waitcnt lgkmcnt(0)
	s_setprio 1
	s_waitcnt lgkmcnt(0)
	v_mfma_scale_f32_16x16x128_f8f6f4 v[78:81], v[2:9], v[148:155], v[78:81], v222, v222 op_sel:[0,1,0] op_sel_hi:[0,0,0]
	v_mfma_scale_f32_16x16x128_f8f6f4 v[74:77], v[10:17], v[148:155], v[74:77], v222, v222 op_sel:[0,1,0] op_sel_hi:[0,0,0]
	v_mfma_scale_f32_16x16x128_f8f6f4 v[62:65], v[2:9], v[156:163], v[62:65], v222, v222 op_sel:[0,1,0] op_sel_hi:[0,0,0]
	v_mfma_scale_f32_16x16x128_f8f6f4 v[58:61], v[10:17], v[156:163], v[58:61], v222, v222 op_sel:[0,1,0] op_sel_hi:[0,0,0]
	v_mfma_scale_f32_16x16x128_f8f6f4 v[46:49], v[2:9], v[164:171], v[46:49], v222, v222 op_sel:[0,1,0] op_sel_hi:[0,0,0]
	v_mfma_scale_f32_16x16x128_f8f6f4 v[42:45], v[10:17], v[164:171], v[42:45], v222, v222 op_sel:[0,1,0] op_sel_hi:[0,0,0]
	v_mfma_scale_f32_16x16x128_f8f6f4 v[30:33], v[2:9], v[172:179], v[30:33], v222, v222 op_sel:[0,1,0] op_sel_hi:[0,0,0]
	v_mfma_scale_f32_16x16x128_f8f6f4 v[26:29], v[10:17], v[172:179], v[26:29], v222, v222 op_sel:[0,1,0] op_sel_hi:[0,0,0]
	s_setprio 0
	s_barrier
	s_add_u32 s34, s42, 0x20000
	s_addc_u32 s35, s43, 0
	s_mov_b64 s[76:77], s[34:35]
	v_mov_b32_e32 v2, v147
	s_mov_b32 m0, s48
	s_add_u32 s34, s34, 0x10000
	global_load_lds_dwordx4 v2, s[76:77]
	s_addc_u32 s35, s35, 0
	v_mov_b32_e32 v2, v147
	s_mov_b32 m0, s49
	s_nop 0
	global_load_lds_dwordx4 v2, s[34:35]
	s_waitcnt vmcnt(6)
	s_barrier
	s_setprio 1
	v_mfma_scale_f32_16x16x128_f8f6f4 v[70:73], v[180:187], v[148:155], v[70:73], v222, v222 op_sel:[0,1,0] op_sel_hi:[0,0,0]
	v_mfma_scale_f32_16x16x128_f8f6f4 v[66:69], v[188:195], v[148:155], v[66:69], v222, v222 op_sel:[0,1,0] op_sel_hi:[0,0,0]
	v_mfma_scale_f32_16x16x128_f8f6f4 v[54:57], v[180:187], v[156:163], v[54:57], v222, v222 op_sel:[0,1,0] op_sel_hi:[0,0,0]
	v_mfma_scale_f32_16x16x128_f8f6f4 v[50:53], v[188:195], v[156:163], v[50:53], v222, v222 op_sel:[0,1,0] op_sel_hi:[0,0,0]
	v_mfma_scale_f32_16x16x128_f8f6f4 v[38:41], v[180:187], v[164:171], v[38:41], v222, v222 op_sel:[0,1,0] op_sel_hi:[0,0,0]
	v_mfma_scale_f32_16x16x128_f8f6f4 v[34:37], v[188:195], v[164:171], v[34:37], v222, v222 op_sel:[0,1,0] op_sel_hi:[0,0,0]
	v_mfma_scale_f32_16x16x128_f8f6f4 v[22:25], v[180:187], v[172:179], v[22:25], v222, v222 op_sel:[0,1,0] op_sel_hi:[0,0,0]
	v_mfma_scale_f32_16x16x128_f8f6f4 v[18:21], v[188:195], v[172:179], v[18:21], v222, v222 op_sel:[0,1,0] op_sel_hi:[0,0,0]
	s_setprio 0
	v_mov_b32_e32 v2, v0
	s_barrier
	v_mov_b32_e32 v6, v0
	v_add_u32_e32 v2, s59, v2
	ds_read_b128 v[2:5], v2
	v_mov_b32_e32 v10, v0
	v_add_u32_e32 v6, s59, v6
	ds_read_b128 v[6:9], v6 offset:1024
	v_mov_b32_e32 v14, v0
	v_add_u32_e32 v10, s59, v10
	ds_read_b128 v[10:13], v10 offset:2048
	s_nop 0
	v_add_u32_e32 v14, s59, v14
	ds_read_b128 v[14:17], v14 offset:3072
	v_mov_b32_e32 v148, v0
	v_mov_b32_e32 v152, v0
	v_add_u32_e32 v148, s56, v148
	ds_read_b128 v[148:151], v148 offset:32768
	v_mov_b32_e32 v156, v0
	v_add_u32_e32 v152, s56, v152
	ds_read_b128 v[152:155], v152 offset:33792
	v_mov_b32_e32 v160, v0
	v_add_u32_e32 v156, s56, v156
	ds_read_b128 v[156:159], v156 offset:34816
	v_mov_b32_e32 v164, v0
	v_add_u32_e32 v160, s56, v160
	ds_read_b128 v[160:163], v160 offset:35840
	v_mov_b32_e32 v168, v0
	v_add_u32_e32 v164, s56, v164
	ds_read_b128 v[164:167], v164 offset:36864
	v_mov_b32_e32 v172, v0
	v_add_u32_e32 v168, s56, v168
	ds_read_b128 v[168:171], v168 offset:37888
	v_mov_b32_e32 v176, v0
	v_add_u32_e32 v172, s56, v172
	s_add_u32 s34, s46, 0x20000
	ds_read_b128 v[172:175], v172 offset:38912
	s_addc_u32 s35, s47, 0
	v_add_u32_e32 v176, s56, v176
	s_mov_b64 s[46:47], s[34:35]
	v_mov_b32_e32 v180, v146
	s_mov_b32 m0, s50
	ds_read_b128 v[176:179], v176 offset:39936
	s_add_u32 s34, s34, 0x10000
	global_load_lds_dwordx4 v180, s[46:47]
	s_addc_u32 s35, s35, 0
	v_mov_b32_e32 v180, v146
	s_mov_b32 m0, s51
	s_nop 0
	global_load_lds_dwordx4 v180, s[34:35]
	s_waitcnt lgkmcnt(8)
	s_barrier
	s_waitcnt lgkmcnt(0)
	s_setprio 1
	s_waitcnt lgkmcnt(0)
	v_mfma_scale_f32_16x16x128_f8f6f4 v[142:145], v[2:9], v[148:155], v[142:145], v222, v222 op_sel:[0,1,0] op_sel_hi:[0,0,0]
	v_mfma_scale_f32_16x16x128_f8f6f4 v[138:141], v[10:17], v[148:155], v[138:141], v222, v222 op_sel:[0,1,0] op_sel_hi:[0,0,0]
	v_mfma_scale_f32_16x16x128_f8f6f4 v[126:129], v[2:9], v[156:163], v[126:129], v222, v222 op_sel:[0,1,0] op_sel_hi:[0,0,0]
	v_mfma_scale_f32_16x16x128_f8f6f4 v[122:125], v[10:17], v[156:163], v[122:125], v222, v222 op_sel:[0,1,0] op_sel_hi:[0,0,0]
	v_mfma_scale_f32_16x16x128_f8f6f4 v[110:113], v[2:9], v[164:171], v[110:113], v222, v222 op_sel:[0,1,0] op_sel_hi:[0,0,0]
	v_mfma_scale_f32_16x16x128_f8f6f4 v[106:109], v[10:17], v[164:171], v[106:109], v222, v222 op_sel:[0,1,0] op_sel_hi:[0,0,0]
	v_mfma_scale_f32_16x16x128_f8f6f4 v[94:97], v[2:9], v[172:179], v[94:97], v222, v222 op_sel:[0,1,0] op_sel_hi:[0,0,0]
	v_mfma_scale_f32_16x16x128_f8f6f4 v[90:93], v[10:17], v[172:179], v[90:93], v222, v222 op_sel:[0,1,0] op_sel_hi:[0,0,0]
	s_setprio 0
	s_barrier
	v_mov_b32_e32 v180, v0
	v_mov_b32_e32 v184, v0
	v_add_u32_e32 v180, s60, v180
	ds_read_b128 v[180:183], v180
	v_mov_b32_e32 v188, v0
	v_add_u32_e32 v184, s60, v184
	ds_read_b128 v[184:187], v184 offset:1024
	v_mov_b32_e32 v192, v0
	v_add_u32_e32 v188, s60, v188
	s_add_u32 s34, s42, 0x80
	ds_read_b128 v[188:191], v188 offset:2048
	s_addc_u32 s35, s43, 0
	v_add_u32_e32 v192, s60, v192
	s_mov_b64 s[46:47], s[34:35]
	v_mov_b32_e32 v196, v147
	s_add_i32 m0, s29, 0x18000
	ds_read_b128 v[192:195], v192 offset:3072
	s_add_u32 s34, s34, 0x10000
	global_load_lds_dwordx4 v196, s[46:47]
	s_addc_u32 s35, s35, 0
	v_mov_b32_e32 v196, v147
	s_add_i32 m0, s29, 0x1a000
	s_nop 0
	global_load_lds_dwordx4 v196, s[34:35]
	s_barrier
	s_waitcnt lgkmcnt(0)
	s_setprio 1
	s_waitcnt lgkmcnt(0)
	v_mfma_scale_f32_16x16x128_f8f6f4 v[134:137], v[180:187], v[148:155], v[134:137], v222, v222 op_sel:[0,1,0] op_sel_hi:[0,0,0]
	v_mfma_scale_f32_16x16x128_f8f6f4 v[130:133], v[188:195], v[148:155], v[130:133], v222, v222 op_sel:[0,1,0] op_sel_hi:[0,0,0]
	v_mfma_scale_f32_16x16x128_f8f6f4 v[118:121], v[180:187], v[156:163], v[118:121], v222, v222 op_sel:[0,1,0] op_sel_hi:[0,0,0]
	v_mfma_scale_f32_16x16x128_f8f6f4 v[114:117], v[188:195], v[156:163], v[114:117], v222, v222 op_sel:[0,1,0] op_sel_hi:[0,0,0]
	v_mfma_scale_f32_16x16x128_f8f6f4 v[102:105], v[180:187], v[164:171], v[102:105], v222, v222 op_sel:[0,1,0] op_sel_hi:[0,0,0]
	v_mfma_scale_f32_16x16x128_f8f6f4 v[98:101], v[188:195], v[164:171], v[98:101], v222, v222 op_sel:[0,1,0] op_sel_hi:[0,0,0]
	v_mfma_scale_f32_16x16x128_f8f6f4 v[86:89], v[180:187], v[172:179], v[86:89], v222, v222 op_sel:[0,1,0] op_sel_hi:[0,0,0]
	v_mfma_scale_f32_16x16x128_f8f6f4 v[82:85], v[188:195], v[172:179], v[82:85], v222, v222 op_sel:[0,1,0] op_sel_hi:[0,0,0]
	s_setprio 0
	v_mov_b32_e32 v148, v0
	s_barrier
	v_mov_b32_e32 v152, v0
	v_add_u32_e32 v148, s56, v148
	ds_read_b128 v[148:151], v148 offset:49152
	v_mov_b32_e32 v156, v0
	v_add_u32_e32 v152, s56, v152
	ds_read_b128 v[152:155], v152 offset:50176
	v_mov_b32_e32 v160, v0
	v_add_u32_e32 v156, s56, v156
	ds_read_b128 v[156:159], v156 offset:51200
	v_mov_b32_e32 v164, v0
	v_add_u32_e32 v160, s56, v160
	ds_read_b128 v[160:163], v160 offset:52224
	v_mov_b32_e32 v168, v0
	v_add_u32_e32 v164, s56, v164
	ds_read_b128 v[164:167], v164 offset:53248
	v_mov_b32_e32 v172, v0
	v_add_u32_e32 v168, s56, v168
	ds_read_b128 v[168:171], v168 offset:54272
	v_mov_b32_e32 v176, v0
	v_add_u32_e32 v172, s56, v172
	ds_read_b128 v[172:175], v172 offset:55296
	s_mov_b64 s[34:35], s[44:45]
	v_add_u32_e32 v176, s56, v176
	s_mov_b32 m0, s53
	ds_read_b128 v[176:179], v176 offset:56320
	v_mov_b32_e32 v196, v146
	s_nop 0
	global_load_lds_dwordx4 v196, s[34:35]
	s_add_u32 s34, s44, 0x10000
	s_addc_u32 s35, s45, 0
	v_mov_b32_e32 v196, v146
	s_mov_b32 m0, s54
	s_nop 0
	global_load_lds_dwordx4 v196, s[34:35]
	s_barrier
	s_waitcnt lgkmcnt(0)
	s_setprio 1
	s_waitcnt lgkmcnt(0)
	v_mfma_scale_f32_16x16x128_f8f6f4 v[78:81], v[2:9], v[148:155], v[78:81], v222, v222 op_sel:[0,1,0] op_sel_hi:[0,0,0]
	v_mfma_scale_f32_16x16x128_f8f6f4 v[74:77], v[10:17], v[148:155], v[74:77], v222, v222 op_sel:[0,1,0] op_sel_hi:[0,0,0]
	v_mfma_scale_f32_16x16x128_f8f6f4 v[62:65], v[2:9], v[156:163], v[62:65], v222, v222 op_sel:[0,1,0] op_sel_hi:[0,0,0]
	v_mfma_scale_f32_16x16x128_f8f6f4 v[58:61], v[10:17], v[156:163], v[58:61], v222, v222 op_sel:[0,1,0] op_sel_hi:[0,0,0]
	v_mfma_scale_f32_16x16x128_f8f6f4 v[46:49], v[2:9], v[164:171], v[46:49], v222, v222 op_sel:[0,1,0] op_sel_hi:[0,0,0]
	v_mfma_scale_f32_16x16x128_f8f6f4 v[42:45], v[10:17], v[164:171], v[42:45], v222, v222 op_sel:[0,1,0] op_sel_hi:[0,0,0]
	v_mfma_scale_f32_16x16x128_f8f6f4 v[30:33], v[2:9], v[172:179], v[30:33], v222, v222 op_sel:[0,1,0] op_sel_hi:[0,0,0]
	v_mfma_scale_f32_16x16x128_f8f6f4 v[26:29], v[10:17], v[172:179], v[26:29], v222, v222 op_sel:[0,1,0] op_sel_hi:[0,0,0]
	s_setprio 0
	s_barrier
	s_add_u32 s34, s42, 0x20080
	s_addc_u32 s35, s43, 0
	s_mov_b64 s[42:43], s[34:35]
	v_mov_b32_e32 v2, v147
	s_add_i32 m0, s29, 0x1c000
	s_add_u32 s34, s34, 0x10000
	global_load_lds_dwordx4 v2, s[42:43]
	s_addc_u32 s35, s35, 0
	v_mov_b32_e32 v2, v147
	s_add_i32 m0, s29, 0x1e000
	s_nop 0
	global_load_lds_dwordx4 v2, s[34:35]
	s_waitcnt vmcnt(6)
	s_barrier
	s_setprio 1
	v_mfma_scale_f32_16x16x128_f8f6f4 v[70:73], v[180:187], v[148:155], v[70:73], v222, v222 op_sel:[0,1,0] op_sel_hi:[0,0,0]
	v_mfma_scale_f32_16x16x128_f8f6f4 v[66:69], v[188:195], v[148:155], v[66:69], v222, v222 op_sel:[0,1,0] op_sel_hi:[0,0,0]
	v_mfma_scale_f32_16x16x128_f8f6f4 v[54:57], v[180:187], v[156:163], v[54:57], v222, v222 op_sel:[0,1,0] op_sel_hi:[0,0,0]
	v_mfma_scale_f32_16x16x128_f8f6f4 v[50:53], v[188:195], v[156:163], v[50:53], v222, v222 op_sel:[0,1,0] op_sel_hi:[0,0,0]
	v_mfma_scale_f32_16x16x128_f8f6f4 v[38:41], v[180:187], v[164:171], v[38:41], v222, v222 op_sel:[0,1,0] op_sel_hi:[0,0,0]
	v_mfma_scale_f32_16x16x128_f8f6f4 v[34:37], v[188:195], v[164:171], v[34:37], v222, v222 op_sel:[0,1,0] op_sel_hi:[0,0,0]
	v_mfma_scale_f32_16x16x128_f8f6f4 v[22:25], v[180:187], v[172:179], v[22:25], v222, v222 op_sel:[0,1,0] op_sel_hi:[0,0,0]
	v_mfma_scale_f32_16x16x128_f8f6f4 v[18:21], v[188:195], v[172:179], v[18:21], v222, v222 op_sel:[0,1,0] op_sel_hi:[0,0,0]
	s_setprio 0
	s_add_i32 s70, s70, 2
	s_add_u32 s68, s68, 0x100
	s_addc_u32 s69, s69, 0
	s_cmp_gt_u32 s70, 5
	s_mov_b64 s[34:35], s[36:37]
	s_barrier
	s_cbranch_scc0 .LBB0_962
	s_lshl_b32 s15, s65, 8
	v_mbcnt_lo_u32_b32 v2, -1, 0
	v_mbcnt_hi_u32_b32 v2, -1, v2
	s_add_i32 s15, s15, s61
	v_and_or_b32 v6, v2, 15, s15
	s_lshl_b32 s15, s64, 8
	v_ashrrev_i32_e32 v2, 1, v2
	s_or_b32 s15, s15, s62
	v_and_b32_e32 v2, -8, v2
	v_add_u32_e32 v4, s15, v2
	v_ashrrev_i32_e32 v7, 31, v6
	v_ashrrev_i32_e32 v5, 31, v4
	v_lshlrev_b64 v[2:3], 10, v[6:7]
	v_lshl_add_u64 v[2:3], v[2:3], 0, v[4:5]
	v_lshlrev_b64 v[2:3], 1, v[2:3]
	v_lshl_add_u64 v[12:13], s[12:13], 0, v[2:3]
	global_load_dwordx4 v[8:11], v[12:13], off
	global_load_dwordx4 v[190:193], v[12:13], off offset:256
	v_or_b32_e32 v216, 16, v6
	v_ashrrev_i32_e32 v217, 31, v216
	v_lshlrev_b64 v[216:217], 10, v[216:217]
	v_lshl_add_u64 v[216:217], v[216:217], 0, v[4:5]
	v_lshlrev_b64 v[216:217], 1, v[216:217]
	v_lshl_add_u64 v[218:219], s[12:13], 0, v[216:217]
	global_load_dwordx4 v[194:197], v[218:219], off
	global_load_dwordx4 v[198:201], v[218:219], off offset:256
	v_or_b32_e32 v216, 32, v6
	v_ashrrev_i32_e32 v217, 31, v216
	v_lshlrev_b64 v[216:217], 10, v[216:217]
	v_lshl_add_u64 v[216:217], v[216:217], 0, v[4:5]
	v_lshlrev_b64 v[216:217], 1, v[216:217]
	v_lshl_add_u64 v[218:219], s[12:13], 0, v[216:217]
	global_load_dwordx4 v[202:205], v[218:219], off
	global_load_dwordx4 v[206:209], v[218:219], off offset:256
	v_or_b32_e32 v216, 48, v6
	v_ashrrev_i32_e32 v217, 31, v216
	v_lshlrev_b64 v[216:217], 10, v[216:217]
	v_lshl_add_u64 v[216:217], v[216:217], 0, v[4:5]
	v_lshlrev_b64 v[216:217], 1, v[216:217]
	v_lshl_add_u64 v[218:219], s[12:13], 0, v[216:217]
	global_load_dwordx4 v[210:213], v[218:219], off
	global_load_dwordx4 v[232:235], v[218:219], off offset:256
	s_mov_b64 s[98:99], 0x40000
	v_lshl_add_u64 v[216:217], v[2:3], 0, s[98:99]
	v_lshl_add_u64 v[218:219], s[12:13], 0, v[216:217]
	global_load_dwordx4 v[236:239], v[218:219], off
	global_load_dwordx4 v[244:247], v[218:219], off offset:256
	s_mov_b64 s[98:99], 0x48000
	v_lshl_add_u64 v[216:217], v[2:3], 0, s[98:99]
	v_lshl_add_u64 v[218:219], s[12:13], 0, v[216:217]
	global_load_dwordx4 v[248:251], v[218:219], off
	global_load_dwordx4 v[148:151], v[218:219], off offset:256
	s_mov_b64 s[98:99], 0x50000
	v_lshl_add_u64 v[216:217], v[2:3], 0, s[98:99]
	v_lshl_add_u64 v[218:219], s[12:13], 0, v[216:217]
	global_load_dwordx4 v[154:157], v[218:219], off
	global_load_dwordx4 v[166:169], v[218:219], off offset:256
	s_mov_b64 s[98:99], 0x58000
	v_lshl_add_u64 v[216:217], v[2:3], 0, s[98:99]
	v_lshl_add_u64 v[218:219], s[12:13], 0, v[216:217]
	global_load_dwordx4 v[178:181], v[218:219], off
	global_load_dwordx4 v[184:187], v[218:219], off offset:256
	s_mov_b64 s[34:35], 0x40000
	s_and_b64 vcc, exec, s[40:41]
	s_mov_b32 s64, s14
	s_mov_b32 s65, s16
	s_mov_b64 s[36:37], s[30:31]
	s_waitcnt vmcnt(15)
	v_lshlrev_b32_e32 v14, 16, v8
	v_and_b32_e32 v15, 0xffff0000, v8
	v_pk_fma_f32 v[14:15], v[14:15], s[10:11], v[142:143] op_sel_hi:[1,0,1]
	s_nop 0
	v_cvt_pk_bf16_f32 v8, v14, v15
	v_lshlrev_b32_e32 v14, 16, v9
	v_and_b32_e32 v15, 0xffff0000, v9
	v_pk_fma_f32 v[14:15], v[14:15], s[10:11], v[144:145] op_sel_hi:[1,0,1]
	s_nop 0
	v_cvt_pk_bf16_f32 v9, v14, v15
	v_lshlrev_b32_e32 v14, 16, v10
	v_and_b32_e32 v15, 0xffff0000, v10
	v_pk_fma_f32 v[14:15], v[14:15], s[10:11], v[138:139] op_sel_hi:[1,0,1]
	s_nop 0
	v_cvt_pk_bf16_f32 v10, v14, v15
	v_lshlrev_b32_e32 v14, 16, v11
	v_and_b32_e32 v15, 0xffff0000, v11
	v_pk_fma_f32 v[14:15], v[14:15], s[10:11], v[140:141] op_sel_hi:[1,0,1]
	s_nop 0
	v_cvt_pk_bf16_f32 v11, v14, v15
	v_lshl_add_u64 v[14:15], s[8:9], 0, v[2:3]
	global_store_dwordx4 v[14:15], v[8:11], off
	s_waitcnt vmcnt(15)
	v_lshlrev_b32_e32 v12, 16, v190
	v_and_b32_e32 v13, 0xffff0000, v190
	v_pk_fma_f32 v[12:13], v[12:13], s[10:11], v[134:135] op_sel_hi:[1,0,1]
	s_nop 0
	v_cvt_pk_bf16_f32 v8, v12, v13
	v_lshlrev_b32_e32 v12, 16, v191
	v_and_b32_e32 v13, 0xffff0000, v191
	v_pk_fma_f32 v[12:13], v[12:13], s[10:11], v[136:137] op_sel_hi:[1,0,1]
	s_nop 0
	v_cvt_pk_bf16_f32 v9, v12, v13
	v_lshlrev_b32_e32 v12, 16, v192
	v_and_b32_e32 v13, 0xffff0000, v192
	v_pk_fma_f32 v[12:13], v[12:13], s[10:11], v[130:131] op_sel_hi:[1,0,1]
	s_nop 0
	v_cvt_pk_bf16_f32 v10, v12, v13
	v_lshlrev_b32_e32 v12, 16, v193
	v_and_b32_e32 v13, 0xffff0000, v193
	v_pk_fma_f32 v[12:13], v[12:13], s[10:11], v[132:133] op_sel_hi:[1,0,1]
	s_nop 0
	v_cvt_pk_bf16_f32 v11, v12, v13
	global_store_dwordx4 v[14:15], v[8:11], off offset:256
	s_nop 1
	v_or_b32_e32 v8, 16, v6
	v_ashrrev_i32_e32 v9, 31, v8
	v_lshlrev_b64 v[8:9], 10, v[8:9]
	v_lshl_add_u64 v[8:9], v[8:9], 0, v[4:5]
	v_lshlrev_b64 v[12:13], 1, v[8:9]
	v_lshl_add_u64 v[14:15], s[12:13], 0, v[12:13]
	v_lshl_add_u64 v[12:13], s[8:9], 0, v[12:13]
	s_waitcnt vmcnt(15)
	v_lshlrev_b32_e32 v16, 16, v194
	v_and_b32_e32 v17, 0xffff0000, v194
	v_pk_fma_f32 v[16:17], v[16:17], s[10:11], v[126:127] op_sel_hi:[1,0,1]
	s_nop 0
	v_cvt_pk_bf16_f32 v8, v16, v17
	v_lshlrev_b32_e32 v16, 16, v195
	v_and_b32_e32 v17, 0xffff0000, v195
	v_pk_fma_f32 v[16:17], v[16:17], s[10:11], v[128:129] op_sel_hi:[1,0,1]
	s_nop 0
	v_cvt_pk_bf16_f32 v9, v16, v17
	v_lshlrev_b32_e32 v16, 16, v196
	v_and_b32_e32 v17, 0xffff0000, v196
	v_pk_fma_f32 v[16:17], v[16:17], s[10:11], v[122:123] op_sel_hi:[1,0,1]
	s_nop 0
	v_cvt_pk_bf16_f32 v10, v16, v17
	v_lshlrev_b32_e32 v16, 16, v197
	v_and_b32_e32 v17, 0xffff0000, v197
	v_pk_fma_f32 v[16:17], v[16:17], s[10:11], v[124:125] op_sel_hi:[1,0,1]
	s_nop 0
	v_cvt_pk_bf16_f32 v11, v16, v17
	global_store_dwordx4 v[12:13], v[8:11], off
	s_waitcnt vmcnt(15)
	v_lshlrev_b32_e32 v14, 16, v198
	v_and_b32_e32 v15, 0xffff0000, v198
	v_pk_fma_f32 v[14:15], v[14:15], s[10:11], v[118:119] op_sel_hi:[1,0,1]
	s_nop 0
	v_cvt_pk_bf16_f32 v8, v14, v15
	v_lshlrev_b32_e32 v14, 16, v199
	v_and_b32_e32 v15, 0xffff0000, v199
	v_pk_fma_f32 v[14:15], v[14:15], s[10:11], v[120:121] op_sel_hi:[1,0,1]
	s_nop 0
	v_cvt_pk_bf16_f32 v9, v14, v15
	v_lshlrev_b32_e32 v14, 16, v200
	v_and_b32_e32 v15, 0xffff0000, v200
	v_pk_fma_f32 v[14:15], v[14:15], s[10:11], v[114:115] op_sel_hi:[1,0,1]
	s_nop 0
	v_cvt_pk_bf16_f32 v10, v14, v15
	v_lshlrev_b32_e32 v14, 16, v201
	v_and_b32_e32 v15, 0xffff0000, v201
	v_pk_fma_f32 v[14:15], v[14:15], s[10:11], v[116:117] op_sel_hi:[1,0,1]
	s_nop 0
	v_cvt_pk_bf16_f32 v11, v14, v15
	global_store_dwordx4 v[12:13], v[8:11], off offset:256
	s_nop 1
	v_or_b32_e32 v8, 32, v6
	v_ashrrev_i32_e32 v9, 31, v8
	v_lshlrev_b64 v[8:9], 10, v[8:9]
	v_lshl_add_u64 v[8:9], v[8:9], 0, v[4:5]
	v_lshlrev_b64 v[12:13], 1, v[8:9]
	v_lshl_add_u64 v[14:15], s[12:13], 0, v[12:13]
	v_lshl_add_u64 v[12:13], s[8:9], 0, v[12:13]
	v_or_b32_e32 v6, 48, v6
	v_ashrrev_i32_e32 v7, 31, v6
	v_lshlrev_b64 v[6:7], 10, v[6:7]
	v_lshl_add_u64 v[4:5], v[6:7], 0, v[4:5]
	s_waitcnt vmcnt(15)
	v_lshlrev_b32_e32 v16, 16, v202
	v_and_b32_e32 v17, 0xffff0000, v202
	v_pk_fma_f32 v[16:17], v[16:17], s[10:11], v[110:111] op_sel_hi:[1,0,1]
	s_nop 0
	v_cvt_pk_bf16_f32 v8, v16, v17
	v_lshlrev_b32_e32 v16, 16, v203
	v_and_b32_e32 v17, 0xffff0000, v203
	v_pk_fma_f32 v[16:17], v[16:17], s[10:11], v[112:113] op_sel_hi:[1,0,1]
	s_nop 0
	v_cvt_pk_bf16_f32 v9, v16, v17
	v_lshlrev_b32_e32 v16, 16, v204
	v_and_b32_e32 v17, 0xffff0000, v204
	v_pk_fma_f32 v[16:17], v[16:17], s[10:11], v[106:107] op_sel_hi:[1,0,1]
	s_nop 0
	v_cvt_pk_bf16_f32 v10, v16, v17
	v_lshlrev_b32_e32 v16, 16, v205
	v_and_b32_e32 v17, 0xffff0000, v205
	v_pk_fma_f32 v[16:17], v[16:17], s[10:11], v[108:109] op_sel_hi:[1,0,1]
	s_nop 0
	v_cvt_pk_bf16_f32 v11, v16, v17
	global_store_dwordx4 v[12:13], v[8:11], off
	s_waitcnt vmcnt(15)
	v_lshlrev_b32_e32 v14, 16, v206
	v_and_b32_e32 v15, 0xffff0000, v206
	v_pk_fma_f32 v[14:15], v[14:15], s[10:11], v[102:103] op_sel_hi:[1,0,1]
	s_nop 0
	v_cvt_pk_bf16_f32 v8, v14, v15
	v_lshlrev_b32_e32 v14, 16, v207
	v_and_b32_e32 v15, 0xffff0000, v207
	v_pk_fma_f32 v[14:15], v[14:15], s[10:11], v[104:105] op_sel_hi:[1,0,1]
	s_nop 0
	v_cvt_pk_bf16_f32 v9, v14, v15
	v_lshlrev_b32_e32 v14, 16, v208
	v_and_b32_e32 v15, 0xffff0000, v208
	v_pk_fma_f32 v[14:15], v[14:15], s[10:11], v[98:99] op_sel_hi:[1,0,1]
	s_nop 0
	v_cvt_pk_bf16_f32 v10, v14, v15
	v_lshlrev_b32_e32 v14, 16, v209
	v_and_b32_e32 v15, 0xffff0000, v209
	v_pk_fma_f32 v[14:15], v[14:15], s[10:11], v[100:101] op_sel_hi:[1,0,1]
	s_nop 0
	v_cvt_pk_bf16_f32 v11, v14, v15
	global_store_dwordx4 v[12:13], v[8:11], off offset:256
	s_nop 1
	v_lshlrev_b64 v[8:9], 1, v[4:5]
	v_lshl_add_u64 v[10:11], s[12:13], 0, v[8:9]
	v_lshl_add_u64 v[8:9], s[8:9], 0, v[8:9]
	s_waitcnt vmcnt(15)
	v_lshlrev_b32_e32 v12, 16, v210
	v_and_b32_e32 v13, 0xffff0000, v210
	v_pk_fma_f32 v[12:13], v[12:13], s[10:11], v[94:95] op_sel_hi:[1,0,1]
	s_nop 0
	v_cvt_pk_bf16_f32 v4, v12, v13
	v_lshlrev_b32_e32 v12, 16, v211
	v_and_b32_e32 v13, 0xffff0000, v211
	v_pk_fma_f32 v[12:13], v[12:13], s[10:11], v[96:97] op_sel_hi:[1,0,1]
	s_nop 0
	v_cvt_pk_bf16_f32 v5, v12, v13
	v_lshlrev_b32_e32 v12, 16, v212
	v_and_b32_e32 v13, 0xffff0000, v212
	v_pk_fma_f32 v[12:13], v[12:13], s[10:11], v[90:91] op_sel_hi:[1,0,1]
	s_nop 0
	v_cvt_pk_bf16_f32 v6, v12, v13
	v_lshlrev_b32_e32 v12, 16, v213
	v_and_b32_e32 v13, 0xffff0000, v213
	v_pk_fma_f32 v[12:13], v[12:13], s[10:11], v[92:93] op_sel_hi:[1,0,1]
	s_nop 0
	v_cvt_pk_bf16_f32 v7, v12, v13
	global_store_dwordx4 v[8:9], v[4:7], off
	s_waitcnt vmcnt(15)
	v_lshlrev_b32_e32 v10, 16, v232
	v_and_b32_e32 v11, 0xffff0000, v232
	v_pk_fma_f32 v[10:11], v[10:11], s[10:11], v[86:87] op_sel_hi:[1,0,1]
	s_nop 0
	v_cvt_pk_bf16_f32 v4, v10, v11
	v_lshlrev_b32_e32 v10, 16, v233
	v_and_b32_e32 v11, 0xffff0000, v233
	v_pk_fma_f32 v[10:11], v[10:11], s[10:11], v[88:89] op_sel_hi:[1,0,1]
	s_nop 0
	v_cvt_pk_bf16_f32 v5, v10, v11
	v_lshlrev_b32_e32 v10, 16, v234
	v_and_b32_e32 v11, 0xffff0000, v234
	v_pk_fma_f32 v[10:11], v[10:11], s[10:11], v[82:83] op_sel_hi:[1,0,1]
	s_nop 0
	v_cvt_pk_bf16_f32 v6, v10, v11
	v_lshlrev_b32_e32 v10, 16, v235
	v_and_b32_e32 v11, 0xffff0000, v235
	v_pk_fma_f32 v[10:11], v[10:11], s[10:11], v[84:85] op_sel_hi:[1,0,1]
	s_nop 0
	v_cvt_pk_bf16_f32 v7, v10, v11
	global_store_dwordx4 v[8:9], v[4:7], off offset:256
	v_lshl_add_u64 v[8:9], v[2:3], 0, s[34:35]
	v_lshl_add_u64 v[10:11], s[12:13], 0, v[8:9]
	v_lshl_add_u64 v[8:9], s[8:9], 0, v[8:9]
	s_mov_b64 s[34:35], 0x48000
	s_waitcnt vmcnt(15)
	v_lshlrev_b32_e32 v12, 16, v236
	v_and_b32_e32 v13, 0xffff0000, v236
	v_pk_fma_f32 v[12:13], v[12:13], s[10:11], v[78:79] op_sel_hi:[1,0,1]
	s_nop 0
	v_cvt_pk_bf16_f32 v4, v12, v13
	v_lshlrev_b32_e32 v12, 16, v237
	v_and_b32_e32 v13, 0xffff0000, v237
	v_pk_fma_f32 v[12:13], v[12:13], s[10:11], v[80:81] op_sel_hi:[1,0,1]
	s_nop 0
	v_cvt_pk_bf16_f32 v5, v12, v13
	v_lshlrev_b32_e32 v12, 16, v238
	v_and_b32_e32 v13, 0xffff0000, v238
	v_pk_fma_f32 v[12:13], v[12:13], s[10:11], v[74:75] op_sel_hi:[1,0,1]
	s_nop 0
	v_cvt_pk_bf16_f32 v6, v12, v13
	v_lshlrev_b32_e32 v12, 16, v239
	v_and_b32_e32 v13, 0xffff0000, v239
	v_pk_fma_f32 v[12:13], v[12:13], s[10:11], v[76:77] op_sel_hi:[1,0,1]
	s_nop 0
	v_cvt_pk_bf16_f32 v7, v12, v13
	global_store_dwordx4 v[8:9], v[4:7], off
	s_waitcnt vmcnt(15)
	v_lshlrev_b32_e32 v10, 16, v244
	v_and_b32_e32 v11, 0xffff0000, v244
	v_pk_fma_f32 v[10:11], v[10:11], s[10:11], v[70:71] op_sel_hi:[1,0,1]
	s_nop 0
	v_cvt_pk_bf16_f32 v4, v10, v11
	v_lshlrev_b32_e32 v10, 16, v245
	v_and_b32_e32 v11, 0xffff0000, v245
	v_pk_fma_f32 v[10:11], v[10:11], s[10:11], v[72:73] op_sel_hi:[1,0,1]
	s_nop 0
	v_cvt_pk_bf16_f32 v5, v10, v11
	v_lshlrev_b32_e32 v10, 16, v246
	v_and_b32_e32 v11, 0xffff0000, v246
	v_pk_fma_f32 v[10:11], v[10:11], s[10:11], v[66:67] op_sel_hi:[1,0,1]
	s_nop 0
	v_cvt_pk_bf16_f32 v6, v10, v11
	v_lshlrev_b32_e32 v10, 16, v247
	v_and_b32_e32 v11, 0xffff0000, v247
	v_pk_fma_f32 v[10:11], v[10:11], s[10:11], v[68:69] op_sel_hi:[1,0,1]
	s_nop 0
	v_cvt_pk_bf16_f32 v7, v10, v11
	global_store_dwordx4 v[8:9], v[4:7], off offset:256
	v_lshl_add_u64 v[8:9], v[2:3], 0, s[34:35]
	v_lshl_add_u64 v[10:11], s[12:13], 0, v[8:9]
	v_lshl_add_u64 v[8:9], s[8:9], 0, v[8:9]
	s_mov_b64 s[34:35], 0x50000
	s_waitcnt vmcnt(15)
	v_lshlrev_b32_e32 v12, 16, v248
	v_and_b32_e32 v13, 0xffff0000, v248
	v_pk_fma_f32 v[12:13], v[12:13], s[10:11], v[62:63] op_sel_hi:[1,0,1]
	s_nop 0
	v_cvt_pk_bf16_f32 v4, v12, v13
	v_lshlrev_b32_e32 v12, 16, v249
	v_and_b32_e32 v13, 0xffff0000, v249
	v_pk_fma_f32 v[12:13], v[12:13], s[10:11], v[64:65] op_sel_hi:[1,0,1]
	s_nop 0
	v_cvt_pk_bf16_f32 v5, v12, v13
	v_lshlrev_b32_e32 v12, 16, v250
	v_and_b32_e32 v13, 0xffff0000, v250
	v_pk_fma_f32 v[12:13], v[12:13], s[10:11], v[58:59] op_sel_hi:[1,0,1]
	s_nop 0
	v_cvt_pk_bf16_f32 v6, v12, v13
	v_lshlrev_b32_e32 v12, 16, v251
	v_and_b32_e32 v13, 0xffff0000, v251
	v_pk_fma_f32 v[12:13], v[12:13], s[10:11], v[60:61] op_sel_hi:[1,0,1]
	s_nop 0
	v_cvt_pk_bf16_f32 v7, v12, v13
	global_store_dwordx4 v[8:9], v[4:7], off
	s_waitcnt vmcnt(15)
	v_lshlrev_b32_e32 v10, 16, v148
	v_and_b32_e32 v11, 0xffff0000, v148
	v_pk_fma_f32 v[10:11], v[10:11], s[10:11], v[54:55] op_sel_hi:[1,0,1]
	s_nop 0
	v_cvt_pk_bf16_f32 v4, v10, v11
	v_lshlrev_b32_e32 v10, 16, v149
	v_and_b32_e32 v11, 0xffff0000, v149
	v_pk_fma_f32 v[10:11], v[10:11], s[10:11], v[56:57] op_sel_hi:[1,0,1]
	s_nop 0
	v_cvt_pk_bf16_f32 v5, v10, v11
	v_lshlrev_b32_e32 v10, 16, v150
	v_and_b32_e32 v11, 0xffff0000, v150
	v_pk_fma_f32 v[10:11], v[10:11], s[10:11], v[50:51] op_sel_hi:[1,0,1]
	s_nop 0
	v_cvt_pk_bf16_f32 v6, v10, v11
	v_lshlrev_b32_e32 v10, 16, v151
	v_and_b32_e32 v11, 0xffff0000, v151
	v_pk_fma_f32 v[10:11], v[10:11], s[10:11], v[52:53] op_sel_hi:[1,0,1]
	s_nop 0
	v_cvt_pk_bf16_f32 v7, v10, v11
	global_store_dwordx4 v[8:9], v[4:7], off offset:256
	v_lshl_add_u64 v[8:9], v[2:3], 0, s[34:35]
	v_lshl_add_u64 v[10:11], s[12:13], 0, v[8:9]
	v_lshl_add_u64 v[8:9], s[8:9], 0, v[8:9]
	s_mov_b64 s[34:35], 0x58000
	s_waitcnt vmcnt(15)
	v_lshlrev_b32_e32 v12, 16, v154
	v_and_b32_e32 v13, 0xffff0000, v154
	v_pk_fma_f32 v[12:13], v[12:13], s[10:11], v[46:47] op_sel_hi:[1,0,1]
	s_nop 0
	v_cvt_pk_bf16_f32 v4, v12, v13
	v_lshlrev_b32_e32 v12, 16, v155
	v_and_b32_e32 v13, 0xffff0000, v155
	v_pk_fma_f32 v[12:13], v[12:13], s[10:11], v[48:49] op_sel_hi:[1,0,1]
	s_nop 0
	v_cvt_pk_bf16_f32 v5, v12, v13
	v_lshlrev_b32_e32 v12, 16, v156
	v_and_b32_e32 v13, 0xffff0000, v156
	v_pk_fma_f32 v[12:13], v[12:13], s[10:11], v[42:43] op_sel_hi:[1,0,1]
	s_nop 0
	v_cvt_pk_bf16_f32 v6, v12, v13
	v_lshlrev_b32_e32 v12, 16, v157
	v_and_b32_e32 v13, 0xffff0000, v157
	v_pk_fma_f32 v[12:13], v[12:13], s[10:11], v[44:45] op_sel_hi:[1,0,1]
	s_nop 0
	v_cvt_pk_bf16_f32 v7, v12, v13
	global_store_dwordx4 v[8:9], v[4:7], off
	s_waitcnt vmcnt(15)
	v_lshlrev_b32_e32 v10, 16, v166
	v_and_b32_e32 v11, 0xffff0000, v166
	v_pk_fma_f32 v[10:11], v[10:11], s[10:11], v[38:39] op_sel_hi:[1,0,1]
	s_nop 0
	v_cvt_pk_bf16_f32 v4, v10, v11
	v_lshlrev_b32_e32 v10, 16, v167
	v_and_b32_e32 v11, 0xffff0000, v167
	v_pk_fma_f32 v[10:11], v[10:11], s[10:11], v[40:41] op_sel_hi:[1,0,1]
	s_nop 0
	v_cvt_pk_bf16_f32 v5, v10, v11
	v_lshlrev_b32_e32 v10, 16, v168
	v_and_b32_e32 v11, 0xffff0000, v168
	v_pk_fma_f32 v[10:11], v[10:11], s[10:11], v[34:35] op_sel_hi:[1,0,1]
	s_nop 0
	v_cvt_pk_bf16_f32 v6, v10, v11
	v_lshlrev_b32_e32 v10, 16, v169
	v_and_b32_e32 v11, 0xffff0000, v169
	v_pk_fma_f32 v[10:11], v[10:11], s[10:11], v[36:37] op_sel_hi:[1,0,1]
	s_nop 0
	v_cvt_pk_bf16_f32 v7, v10, v11
	global_store_dwordx4 v[8:9], v[4:7], off offset:256
	s_nop 1
	v_lshl_add_u64 v[6:7], v[2:3], 0, s[34:35]
	v_lshl_add_u64 v[8:9], s[12:13], 0, v[6:7]
	v_lshl_add_u64 v[6:7], s[8:9], 0, v[6:7]
	s_mov_b64 s[34:35], s[18:19]
	s_waitcnt vmcnt(15)
	v_lshlrev_b32_e32 v10, 16, v178
	v_and_b32_e32 v11, 0xffff0000, v178
	v_pk_fma_f32 v[10:11], v[10:11], s[10:11], v[30:31] op_sel_hi:[1,0,1]
	s_nop 0
	v_cvt_pk_bf16_f32 v2, v10, v11
	v_lshlrev_b32_e32 v10, 16, v179
	v_and_b32_e32 v11, 0xffff0000, v179
	v_pk_fma_f32 v[10:11], v[10:11], s[10:11], v[32:33] op_sel_hi:[1,0,1]
	s_nop 0
	v_cvt_pk_bf16_f32 v3, v10, v11
	v_lshlrev_b32_e32 v10, 16, v180
	v_and_b32_e32 v11, 0xffff0000, v180
	v_pk_fma_f32 v[10:11], v[10:11], s[10:11], v[26:27] op_sel_hi:[1,0,1]
	s_nop 0
	v_cvt_pk_bf16_f32 v4, v10, v11
	v_lshlrev_b32_e32 v10, 16, v181
	v_and_b32_e32 v11, 0xffff0000, v181
	v_pk_fma_f32 v[10:11], v[10:11], s[10:11], v[28:29] op_sel_hi:[1,0,1]
	s_nop 0
	v_cvt_pk_bf16_f32 v5, v10, v11
	global_store_dwordx4 v[6:7], v[2:5], off
	s_waitcnt vmcnt(15)
	v_lshlrev_b32_e32 v8, 16, v184
	v_and_b32_e32 v9, 0xffff0000, v184
	v_pk_fma_f32 v[8:9], v[8:9], s[10:11], v[22:23] op_sel_hi:[1,0,1]
	s_nop 0
	v_cvt_pk_bf16_f32 v2, v8, v9
	v_lshlrev_b32_e32 v8, 16, v185
	v_and_b32_e32 v9, 0xffff0000, v185
	v_pk_fma_f32 v[8:9], v[8:9], s[10:11], v[24:25] op_sel_hi:[1,0,1]
	s_nop 0
	v_cvt_pk_bf16_f32 v3, v8, v9
	v_lshlrev_b32_e32 v8, 16, v186
	v_and_b32_e32 v9, 0xffff0000, v186
	v_pk_fma_f32 v[8:9], v[8:9], s[10:11], v[18:19] op_sel_hi:[1,0,1]
	s_nop 0
	v_cvt_pk_bf16_f32 v4, v8, v9
	v_lshlrev_b32_e32 v8, 16, v187
	v_and_b32_e32 v9, 0xffff0000, v187
	v_pk_fma_f32 v[8:9], v[8:9], s[10:11], v[20:21] op_sel_hi:[1,0,1]
	s_nop 0
	v_cvt_pk_bf16_f32 v5, v8, v9
	global_store_dwordx4 v[6:7], v[2:5], off offset:256
	s_cbranch_vccz .LBB0_955
	s_waitcnt vmcnt(0)
	s_cmpk_gt_u32 s2, 0xff
	s_cbranch_scc1 .LBB0_966
	s_barrier
